# stack plus cross-attention: LDS operand reads double-buffered one MFMA ahead (38 serialized read-wait-MFMA steps)
# baseline (speedup 1.0000x reference)
; #define LAS __attribute__((address_space(3)))
; __device__ __forceinline__ int otid(int wv) { int t = wv * 64 + lane_id(); asm volatile("" : "+v"(t)); return t; }
; __device__ __forceinline__ int v_st(int k, int c) { const int kk = (k & ~0xC) | ((k & 4) << 1) | ((k & 8) >> 1); return ((kk >> 3) * 4 + (c >> 5)) * 512 + ((kk & 7) * 32 + (c & 31)) * 2; }
; __device__ __forceinline__ int v_rd_base(int lane) { return ((lane & 3) << 3) | (((lane >> 2) & 3) << 6) | (((lane >> 4) & 1) << 5) | (((lane >> 5) & 1) << 8); }
; #define ATT_LOAD(X, t) do { const int _j = 64 * (t) + sr; ks##X##0 = *(const bf16x8*)(c.k_ptr(_j) + sc); vs##X##0 = *(const bf16x8*)(c.v_ptr(_j) + sc); \
;         if (D128) { ks##X##1 = *(const bf16x8*)(c.k_ptr(_j + 32) + sc); vs##X##1 = *(const bf16x8*)(c.v_ptr(_j + 32) + sc); } } while (0)
; template <int DK16, int DV32, bool MASK, int HALFWIN, bool RES, bool WT, class P>
; __device__ __forceinline__ void attn_unit(LAS unsigned char* lds, const P& c, const int ntiles, const float C, const int wv) {
;     const int tid = otid(wv), wid = __builtin_amdgcn_readfirstlane(tid >> 6), lane = tid & 63, r32 = lane & 31, hi = lane >> 5;
;     constexpr int NB = RES ? 4 : 2;
;     LAS unsigned char* V_lds = lds; LAS unsigned char* K_lds = lds + NB * SHM_T;
;     LAS float* wsf = (LAS float*)(lds + (RES ? 132096 : OFF_WS)) + wid * 64; LAS float* li_l = wsf; LAS float* al_l = wsf + 32;
;     bf16x8 qr[DK16];
;     { const bf16* qp = c.q_ptr(wid, r32) + hi * 8;
; #pragma unroll
;       for (int d0 = 0; d0 < DK16; ++d0) qr[d0] = *(const bf16x8*)(qp + d0 * 16); }
;     float m_reg = c.m0(wid), l_reg = c.l0(wid);
;     f32x16 o[DV32];
; #pragma unroll
;     for (int d = 0; d < DV32; ++d)
; #pragma unroll
;         for (int r = 0; r < 16; ++r) o[d][r] = 0.f;
;     constexpr bool D128 = (DK16 == 8);
;     const int sr = D128 ? (tid >> 4) : (tid >> 3), sc = D128 ? (tid & 15) * 8 : (tid & 7) * 8;
;     const int vst0 = v_st(sr, sc), vst1 = v_st(32 + sr, sc), kst0 = ATT_KSWZ(sr, sc * 2), kst1 = ATT_KSWZ(32 + sr, sc * 2);
;     const int vb0 = (int)(unsigned)(uintptr_t)V_lds + v_rd_base(lane);
;     bf16x8 ksA0, ksA1, vsA0, vsA1, ksB0, ksB1, vsB0, vsB1;
;     ...
;     if constexpr (RES) {
;         ATT_LOAD(A, 0); ATT_LOAD(B, 1); ATT_WRITE(A, 0); ATT_LOAD(A, 2); ATT_WRITE(B, 1); ATT_LOAD(B, 3); ATT_WRITE(A, 2); ATT_WRITE(B, 3);
;         __syncthreads();
.LBB0_1197:
	s_ashr_i32 s1, s0, 31
	s_lshl_b64 s[0:1], s[0:1], 19
	s_add_u32 s0, s6, s0
	s_addc_u32 s1, s7, s1
	s_barrier
	v_mbcnt_lo_u32_b32 v0, -1, 0
	v_mbcnt_hi_u32_b32 v0, -1, v0
	s_add_u32 s0, s0, 0x21700000
	v_add_u32_e32 v154, s93, v0
	s_addc_u32 s1, s1, 0
	s_waitcnt lgkmcnt(0)
	v_readfirstlane_b32 s3, v154
	s_lshl_b32 s8, s17, 8
	s_ashr_i32 s11, s3, 6
	v_and_b32_e32 v156, 31, v154
	s_lshl_b32 s3, s11, 8
	s_lshl_b32 s9, s11, 5
	v_or_b32_e32 v0, s8, v156
	s_and_b32 s2, s16, 0xffffff80
	s_add_i32 s10, s3, 0x100
	v_add_u32_e32 v0, s9, v0
	s_lshl_b32 s3, s15, 8
	v_ashrrev_i32_e32 v1, 31, v0
	s_add_i32 s2, s3, s2
	v_lshlrev_b64 v[0:1], 10, v[0:1]
	s_ashr_i32 s3, s2, 31
	v_lshl_add_u64 v[0:1], s[6:7], 0, v[0:1]
	s_lshl_b64 s[4:5], s[2:3], 1
	v_lshrrev_b32_e32 v32, 1, v154
	v_lshl_add_u64 v[0:1], v[0:1], 0, s[4:5]
	v_and_b32_e32 v64, 16, v32
	v_lshl_add_u64 v[0:1], v[0:1], 0, v[64:65]
	s_mov_b64 s[16:17], 0x8100000
	s_mov_b32 s15, 0x8100000
	v_lshl_add_u64 v[2:3], v[0:1], 0, s[16:17]
	v_add_co_u32_e32 v0, vcc, s15, v0
	v_mov_b32_e32 v9, v65
	s_nop 0
	v_addc_co_u32_e32 v1, vcc, 0, v1, vcc
	global_load_dwordx4 v[126:129], v[0:1], off
	global_load_dwordx4 v[122:125], v[2:3], off offset:32
	global_load_dwordx4 v[118:121], v[2:3], off offset:64
	global_load_dwordx4 v[114:117], v[2:3], off offset:96
	global_load_dwordx4 v[110:113], v[2:3], off offset:128
	global_load_dwordx4 v[106:109], v[2:3], off offset:160
	global_load_dwordx4 v[102:105], v[2:3], off offset:192
	global_load_dwordx4 v[98:101], v[2:3], off offset:224
	v_ashrrev_i32_e32 v0, 4, v154
	v_and_b32_e32 v3, 0xfffff0, v0
	v_lshlrev_b32_e32 v4, 1, v0
	v_lshlrev_b32_e32 v1, 3, v154
	v_and_or_b32 v3, v4, 8, v3
	v_and_b32_e32 v2, 0x78, v1
	v_lshrrev_b32_e32 v4, 1, v0
	v_lshrrev_b32_e32 v3, 1, v3
	v_bfe_u32 v1, v1, 5, 2
	v_and_b32_e32 v5, 3, v0
	v_or_b32_e32 v3, v3, v1
	v_and_or_b32 v4, v4, 4, v5
	v_lshlrev_b32_e32 v8, 1, v2
	v_lshlrev_b32_e32 v3, 9, v3
	v_lshlrev_b32_e32 v4, 6, v4
	v_and_b32_e32 v2, 48, v8
	v_add_u32_e32 v10, 32, v0
	v_or3_b32 v33, v3, v4, v2
	v_and_b32_e32 v3, 0xfffff0, v10
	v_lshlrev_b32_e32 v5, 1, v10
	v_and_or_b32 v3, v5, 8, v3
	v_lshrrev_b32_e32 v3, 1, v3
	v_or_b32_e32 v1, v3, v1
	v_lshlrev_b32_e32 v1, 9, v1
	v_or3_b32 v36, v1, v4, v2
	v_lshlrev_b32_e32 v1, 8, v0
	v_and_b32_e32 v2, 0x70, v154
	v_bitop3_b32 v37, v8, v1, v2 bitop3:0xde
	v_lshlrev_b32_e32 v1, 8, v10
	v_bitop3_b32 v38, v8, v1, v2 bitop3:0xde
	v_ashrrev_i32_e32 v1, 31, v0
	v_lshlrev_b64 v[0:1], 11, v[0:1]
	v_lshl_add_u64 v[0:1], s[0:1], 0, v[0:1]
	v_ashrrev_i32_e32 v11, 31, v10
	v_lshl_add_u64 v[0:1], v[0:1], 0, s[4:5]
	v_lshlrev_b64 v[10:11], 11, v[10:11]
	v_lshl_add_u64 v[34:35], v[0:1], 0, v[8:9]
	v_lshl_add_u64 v[10:11], s[0:1], 0, v[10:11]
	global_load_dwordx4 v[0:3], v[34:35], off
	global_load_dwordx4 v[4:7], v[34:35], off offset:1024
	v_lshl_add_u64 v[10:11], v[10:11], 0, s[4:5]
	v_lshl_add_u64 v[12:13], v[10:11], 0, v[8:9]
	global_load_dwordx4 v[8:11], v[12:13], off
	s_nop 0
	global_load_dwordx4 v[12:15], v[12:13], off offset:1024
	s_mov_b32 s0, 0x20000
	v_add_co_u32_e32 v16, vcc, s0, v34
	s_mov_b32 s0, 0x30000
	s_nop 0
	v_addc_co_u32_e32 v17, vcc, 0, v35, vcc
	v_lshl_add_u64 v[20:21], v[34:35], 0, s[66:67]
	v_add_co_u32_e32 v24, vcc, s0, v34
	global_load_dwordx4 v[16:19], v[16:17], off
	s_nop 0
	global_load_dwordx4 v[20:23], v[20:21], off offset:1024
	v_lshl_add_u64 v[28:29], v[34:35], 0, s[84:85]
	v_addc_co_u32_e32 v25, vcc, 0, v35, vcc
	global_load_dwordx4 v[24:27], v[24:25], off
	s_nop 0
	global_load_dwordx4 v[28:31], v[28:29], off offset:1024
	v_add_u32_e32 v33, 0x100, v33
	s_add_i32 s46, s91, 0x100
	v_add_u32_e32 v36, 0x100, v36
	s_mov_b32 s0, 0x40000
	s_add_i32 s47, s92, 0x100
	s_add_i32 s52, s65, 0x100
	s_add_i32 s53, s71, 0x100
	v_lshlrev_b32_e32 v168, 8, v156
	v_and_b32_e32 v155, 63, v154
	s_add_i32 s10, s10, 0x20400
	v_cmp_gt_u32_e64 s[4:5], 32, v155
	s_waitcnt vmcnt(6)
	ds_write_b128 v33, v[4:7]
	v_add_u32_e32 v4, s46, v37
	ds_write_b128 v4, v[0:3]
	v_add_u32_e32 v0, s46, v38
	s_waitcnt vmcnt(4)
	ds_write_b128 v36, v[12:15]
	ds_write_b128 v0, v[8:11]
	v_add_co_u32_e32 v0, vcc, s0, v34
	s_mov_b64 s[0:1], 0x50000
	s_nop 0
	v_addc_co_u32_e32 v1, vcc, 0, v35, vcc
	v_lshl_add_u64 v[12:13], v[34:35], 0, s[0:1]
	s_mov_b32 s0, 0x50000
	v_add_co_u32_e32 v8, vcc, s0, v34
	v_lshl_add_u64 v[4:5], v[34:35], 0, s[68:69]
	s_nop 0
	v_addc_co_u32_e32 v9, vcc, 0, v35, vcc
	global_load_dwordx4 v[0:3], v[0:1], off
	s_nop 0
	global_load_dwordx4 v[4:7], v[4:5], off offset:1024
	s_nop 0
	global_load_dwordx4 v[8:11], v[8:9], off
	s_nop 0
	global_load_dwordx4 v[12:15], v[12:13], off offset:1024
	s_waitcnt vmcnt(6)
	ds_write_b128 v33, v[20:23] offset:16384
	v_add_u32_e32 v20, s47, v37
	ds_write_b128 v20, v[16:19]
	s_waitcnt vmcnt(4)
	ds_write_b128 v36, v[28:31] offset:16384
	v_add_u32_e32 v16, s47, v38
	s_mov_b32 s0, 0x60000
	ds_write_b128 v16, v[24:27]
	v_add_co_u32_e32 v16, vcc, s0, v34
	s_mov_b64 s[0:1], 0x70000
	s_nop 0
	v_addc_co_u32_e32 v17, vcc, 0, v35, vcc
	v_lshl_add_u64 v[28:29], v[34:35], 0, s[0:1]
	s_mov_b32 s0, 0x70000
	v_lshl_add_u64 v[20:21], v[34:35], 0, s[62:63]
	v_add_co_u32_e32 v24, vcc, s0, v34
	global_load_dwordx4 v[16:19], v[16:17], off
	s_nop 0
	global_load_dwordx4 v[20:23], v[20:21], off offset:1024
	v_addc_co_u32_e32 v25, vcc, 0, v35, vcc
	global_load_dwordx4 v[24:27], v[24:25], off
	s_nop 0
	global_load_dwordx4 v[28:31], v[28:29], off offset:1024
	s_movk_i32 s0, 0x60
	s_waitcnt vmcnt(6)
	ds_write_b128 v33, v[4:7] offset:32768
	v_add_u32_e32 v4, s52, v37
	ds_write_b128 v4, v[0:3]
	s_waitcnt vmcnt(4)
	ds_write_b128 v36, v[12:15] offset:32768
	v_add_u32_e32 v0, s52, v38
	ds_write_b128 v0, v[8:11]
	s_waitcnt vmcnt(2)
	ds_write_b128 v33, v[20:23] offset:49152
	v_add_u32_e32 v0, s53, v37
	ds_write_b128 v0, v[16:19]
	s_waitcnt vmcnt(0)
	ds_write_b128 v36, v[28:31] offset:49152
	v_add_u32_e32 v0, s53, v38
	ds_write_b128 v0, v[24:27]
	v_lshlrev_b32_e32 v0, 4, v154
	v_and_b32_e32 v0, 0x70, v0
	v_bitop3_b32 v164, v64, v0, s0 bitop3:0x36
	s_movk_i32 s0, 0x80
	v_bitop3_b32 v165, v64, v0, s0 bitop3:0x36
	s_movk_i32 s0, 0xa0
	v_bitop3_b32 v166, v64, v0, s0 bitop3:0x36
	s_movk_i32 s0, 0xc0
	v_bitop3_b32 v167, v64, v0, s0 bitop3:0x36
	s_movk_i32 s0, 0xe0
	v_add_u32_e32 v1, s46, v168
	v_bitop3_b32 v169, v32, v0, 16 bitop3:0x6c
	v_bitop3_b32 v162, v64, v0, 32 bitop3:0x36
	v_bitop3_b32 v163, v64, v0, 64 bitop3:0x36
	v_bitop3_b32 v161, v64, v0, s0 bitop3:0x36
	v_add_u32_e32 v2, v1, v169
	v_add_u32_e32 v20, v1, v162
	v_add_u32_e32 v24, v1, v163
	v_add_u32_e32 v25, v1, v164
	v_add_u32_e32 v26, v1, v165
	v_add_u32_e32 v27, v1, v166
	v_add_u32_e32 v28, v1, v167
	v_add_u32_e32 v29, v1, v161
	s_waitcnt lgkmcnt(0)
	s_barrier
; template <int DK16, int DV32, bool MASK, int HALFWIN, bool RES, bool WT, class P>
; __device__ __forceinline__ void attn_unit(LAS unsigned char* lds, const P& c, const int ntiles, const float C, const int wv) {
;     ...
;             if (do0) {
; #pragma unroll
;                 for (int d0 = 0; d0 < DK16; ++d0) { const bf16x8 b0 = *(const LAS bf16x8*)(Ks + ATT_KSWZ(r32, (d0 * 16 + hi * 8) * 2)); p0 = __builtin_amdgcn_mfma_f32_32x32x16_bf16(b0, qr[d0], p0, 0, 0, 0); } }
;             if (do1) {
; #pragma unroll
;                 for (int d0 = 0; d0 < DK16; ++d0) { const bf16x8 b1 = *(const LAS bf16x8*)(Ks + ATT_KSWZ(32 + r32, (d0 * 16 + hi * 8) * 2)); p1 = __builtin_amdgcn_mfma_f32_32x32x16_bf16(b1, qr[d0], p1, 0, 0, 0); } }
;             if constexpr (MASK) {
;                 const int db = c.dbase(wid, r32, t) + 4 * hi, qi = c.qidx(wid, r32); const unsigned L = (unsigned)c.seqlen(); const bool edge = c.edge();
;                 const LAS float* tb = c.tab(wid) + (db + 2 * HALFWIN);
;     ...
;                 if (do0) ATT_XFORM(p0, 0);
;                 if (do1) ATT_XFORM(p1, 32);
;     ...
;             } else {
; #pragma unroll
;                 for (int r = 0; r < 16; ++r) { p0[r] *= C; p1[r] *= C; }
;             }
;             float pmax = -__builtin_inff();
;             if (do0) {
; #pragma unroll
;                 for (int r = 0; r < 16; ++r) pmax = fmaxf(pmax, p0[r]); }
;             if (do1) {
; #pragma unroll
;                 for (int r = 0; r < 16; ++r) pmax = fmaxf(pmax, p1[r]); }
;             { auto rr = __builtin_amdgcn_permlane32_swap(__float_as_uint(pmax), __float_as_uint(pmax), false, false);
;               pmax = fmaxf(__uint_as_float(rr[0]), __uint_as_float(rr[1])); }
;             const float mn = fmaxf(m_reg, pmax), alpha = __builtin_amdgcn_exp2f(m_reg - mn); m_reg = mn;
;             float ps = 0.f;
;             if (do0) {
; #pragma unroll
;                 for (int r = 0; r < 16; ++r) { p0[r] = __builtin_amdgcn_exp2f(p0[r] - mn); ps += p0[r]; } }
;             if (do1) {
; #pragma unroll
;                 for (int r = 0; r < 16; ++r) { p1[r] = __builtin_amdgcn_exp2f(p1[r] - mn); ps += p1[r]; } }
;             { auto rr = __builtin_amdgcn_permlane32_swap(__float_as_uint(ps), __float_as_uint(ps), false, false);
;               ps = __uint_as_float(rr[0]) + __uint_as_float(rr[1]); }
;             l_reg = l_reg * alpha + ps;
	ds_read_b128 v[16:19], v2
	ds_read_b128 v[32:35], v20
	ds_read_b128 v[36:39], v24
	ds_read_b128 v[40:43], v25
	ds_read_b128 v[44:47], v26
	ds_read_b128 v[48:51], v27
	ds_read_b128 v[52:55], v28
	ds_read_b128 v[56:59], v29
	ds_read_b128 v[0:3], v2 offset:8192
	ds_read_b128 v[20:23], v20 offset:8192
	s_waitcnt lgkmcnt(1)
	v_mfma_f32_32x32x16_bf16 v[0:15], v[0:3], v[126:129], 0
	s_mov_b32 s0, 0xf149f2ca
	s_waitcnt lgkmcnt(0)
	v_mfma_f32_32x32x16_bf16 v[0:15], v[20:23], v[122:125], v[0:15]
	ds_read_b128 v[230:233], v24 offset:8192
	ds_read_b128 v[20:23], v25 offset:8192
	s_waitcnt lgkmcnt(1)
	v_mfma_f32_32x32x16_bf16 v[0:15], v[230:233], v[118:121], v[0:15]
	ds_read_b128 v[230:233], v26 offset:8192
	s_waitcnt lgkmcnt(1)
	v_mfma_f32_32x32x16_bf16 v[0:15], v[20:23], v[114:117], v[0:15]
	ds_read_b128 v[20:23], v27 offset:8192
	s_waitcnt lgkmcnt(1)
	v_mfma_f32_32x32x16_bf16 v[0:15], v[230:233], v[110:113], v[0:15]
	ds_read_b128 v[230:233], v28 offset:8192
	s_waitcnt lgkmcnt(1)
	v_mfma_f32_32x32x16_bf16 v[0:15], v[20:23], v[106:109], v[0:15]
	ds_read_b128 v[20:23], v29 offset:8192
	s_waitcnt lgkmcnt(1)
	v_mfma_f32_32x32x16_bf16 v[0:15], v[230:233], v[102:105], v[0:15]
	s_waitcnt lgkmcnt(0)
	v_mfma_f32_32x32x16_bf16 v[0:15], v[20:23], v[98:101], v[0:15]
	v_mfma_f32_32x32x16_bf16 v[16:31], v[16:19], v[126:129], 0
	s_nop 10
	v_mul_f32_e32 v61, 0x3e0293ee, v14
	v_mul_f32_e32 v63, 0x3e0293ee, v15
	v_mfma_f32_32x32x16_bf16 v[16:31], v[32:35], v[122:125], v[16:31]
	v_mul_f32_e32 v33, 0x3e0293ee, v0
	v_mul_f32_e32 v35, 0x3e0293ee, v1
	v_mfma_f32_32x32x16_bf16 v[16:31], v[36:39], v[118:121], v[16:31]
	v_mul_f32_e32 v37, 0x3e0293ee, v2
	v_mul_f32_e32 v39, 0x3e0293ee, v3
	v_mfma_f32_32x32x16_bf16 v[16:31], v[40:43], v[114:117], v[16:31]
	v_mul_f32_e32 v41, 0x3e0293ee, v4
	v_mul_f32_e32 v43, 0x3e0293ee, v5
	v_mfma_f32_32x32x16_bf16 v[16:31], v[44:47], v[110:113], v[16:31]
	v_mul_f32_e32 v45, 0x3e0293ee, v6
	v_mul_f32_e32 v47, 0x3e0293ee, v7
	v_mfma_f32_32x32x16_bf16 v[16:31], v[48:51], v[106:109], v[16:31]
	v_mul_f32_e32 v49, 0x3e0293ee, v8
	v_mul_f32_e32 v51, 0x3e0293ee, v9
	v_mfma_f32_32x32x16_bf16 v[16:31], v[52:55], v[102:105], v[16:31]
	v_mul_f32_e32 v53, 0x3e0293ee, v10
	v_mul_f32_e32 v55, 0x3e0293ee, v11
	v_mfma_f32_32x32x16_bf16 v[16:31], v[56:59], v[98:101], v[16:31]
	v_mul_f32_e32 v57, 0x3e0293ee, v12
	v_mul_f32_e32 v59, 0x3e0293ee, v13
	s_nop 9
	v_mul_f32_e32 v32, 0x3e0293ee, v16
	v_mul_f32_e32 v34, 0x3e0293ee, v17
	v_mul_f32_e32 v36, 0x3e0293ee, v18
	v_mul_f32_e32 v38, 0x3e0293ee, v19
	v_max3_f32 v32, v32, s38, v34
	v_mul_f32_e32 v40, 0x3e0293ee, v20
	v_mul_f32_e32 v42, 0x3e0293ee, v21
	v_max3_f32 v32, v32, v36, v38
	v_mul_f32_e32 v44, 0x3e0293ee, v22
	v_mul_f32_e32 v46, 0x3e0293ee, v23
	v_max3_f32 v32, v32, v40, v42
	v_mul_f32_e32 v48, 0x3e0293ee, v24
	v_mul_f32_e32 v50, 0x3e0293ee, v25
	v_max3_f32 v32, v32, v44, v46
	v_mul_f32_e32 v52, 0x3e0293ee, v26
	v_mul_f32_e32 v54, 0x3e0293ee, v27
	v_max3_f32 v32, v32, v48, v50
	v_mul_f32_e32 v56, 0x3e0293ee, v28
	v_mul_f32_e32 v58, 0x3e0293ee, v29
	v_max3_f32 v32, v32, v52, v54
	v_mul_f32_e32 v60, 0x3e0293ee, v30
	v_mul_f32_e32 v62, 0x3e0293ee, v31
	v_max3_f32 v32, v32, v56, v58
	v_max3_f32 v32, v32, v60, v62
	v_max3_f32 v32, v32, v33, v35
	v_max3_f32 v32, v32, v37, v39
	v_max3_f32 v32, v32, v41, v43
	v_max3_f32 v32, v32, v45, v47
	v_max3_f32 v32, v32, v49, v51
	v_max3_f32 v32, v32, v53, v55
	v_max3_f32 v32, v32, v57, v59
	v_max3_f32 v32, v32, v61, v63
	v_mov_b32_e32 v33, v32
	s_nop 1
	v_permlane32_swap_b32_e32 v32, v33
	v_max3_f32 v171, v32, v33, s0
	v_fma_f32 v16, v16, s94, -v171
	v_exp_f32_e32 v16, v16
	v_fma_f32 v17, v17, s94, -v171
	v_exp_f32_e32 v17, v17
	v_fma_f32 v18, v18, s94, -v171
	v_exp_f32_e32 v18, v18
	v_fma_f32 v19, v19, s94, -v171
	v_exp_f32_e32 v19, v19
	v_fma_f32 v20, v20, s94, -v171
	v_add_f32_e32 v33, 0, v16
	v_exp_f32_e32 v20, v20
	v_fma_f32 v21, v21, s94, -v171
	v_add_f32_e32 v33, v17, v33
	v_exp_f32_e32 v21, v21
	v_fma_f32 v22, v22, s94, -v171
	v_add_f32_e32 v33, v18, v33
	v_exp_f32_e32 v22, v22
	v_fma_f32 v23, v23, s94, -v171
	v_add_f32_e32 v33, v19, v33
	v_exp_f32_e32 v23, v23
	v_fma_f32 v24, v24, s94, -v171
	v_add_f32_e32 v33, v20, v33
	v_exp_f32_e32 v24, v24
	v_fma_f32 v25, v25, s94, -v171
	v_add_f32_e32 v33, v21, v33
	v_exp_f32_e32 v25, v25
	v_fma_f32 v26, v26, s94, -v171
	v_add_f32_e32 v33, v22, v33
	v_exp_f32_e32 v26, v26
	v_fma_f32 v27, v27, s94, -v171
	v_add_f32_e32 v33, v23, v33
	v_exp_f32_e32 v27, v27
	v_fma_f32 v28, v28, s94, -v171
	v_add_f32_e32 v33, v24, v33
	v_exp_f32_e32 v28, v28
	v_fma_f32 v29, v29, s94, -v171
	v_add_f32_e32 v33, v25, v33
	v_exp_f32_e32 v29, v29
	v_fma_f32 v30, v30, s94, -v171
	v_add_f32_e32 v33, v26, v33
	v_exp_f32_e32 v30, v30
	v_fma_f32 v31, v31, s94, -v171
	v_add_f32_e32 v33, v27, v33
	v_exp_f32_e32 v31, v31
	v_fma_f32 v0, v0, s94, -v171
	v_add_f32_e32 v33, v28, v33
	v_exp_f32_e32 v48, v0
	v_fma_f32 v1, v1, s94, -v171
	v_add_f32_e32 v33, v29, v33
	v_exp_f32_e32 v49, v1
	v_fma_f32 v1, v2, s94, -v171
	v_add_f32_e32 v33, v30, v33
	v_exp_f32_e32 v50, v1
	v_fma_f32 v1, v3, s94, -v171
	v_add_f32_e32 v33, v31, v33
	v_exp_f32_e32 v51, v1
	v_fma_f32 v1, v4, s94, -v171
	v_add_f32_e32 v0, v48, v33
	v_exp_f32_e32 v52, v1
	v_fma_f32 v1, v5, s94, -v171
	v_add_f32_e32 v0, v49, v0
	v_exp_f32_e32 v53, v1
	v_fma_f32 v1, v6, s94, -v171
	v_add_f32_e32 v0, v50, v0
	v_exp_f32_e32 v66, v1
	v_fma_f32 v1, v7, s94, -v171
	v_add_f32_e32 v0, v51, v0
	v_exp_f32_e32 v67, v1
	v_fma_f32 v1, v8, s94, -v171
	v_add_f32_e32 v0, v52, v0
	v_exp_f32_e32 v68, v1
	v_fma_f32 v1, v9, s94, -v171
	v_add_f32_e32 v0, v53, v0
	v_exp_f32_e32 v69, v1
	v_fma_f32 v1, v10, s94, -v171
	v_add_f32_e32 v0, v66, v0
	v_exp_f32_e32 v70, v1
	v_fma_f32 v1, v11, s94, -v171
	v_add_f32_e32 v0, v67, v0
	v_exp_f32_e32 v71, v1
	v_fma_f32 v1, v12, s94, -v171
	v_add_f32_e32 v0, v68, v0
	v_exp_f32_e32 v72, v1
	v_fma_f32 v1, v13, s94, -v171
	v_add_f32_e32 v0, v69, v0
	v_exp_f32_e32 v73, v1
	v_fma_f32 v1, v14, s94, -v171
	v_add_f32_e32 v0, v70, v0
	v_exp_f32_e32 v74, v1
	v_fma_f32 v1, v15, s94, -v171
	v_add_f32_e32 v0, v71, v0
	v_exp_f32_e32 v75, v1
	v_sub_f32_e32 v32, 0xf149f2ca, v171
	v_add_f32_e32 v0, v72, v0
	v_add_f32_e32 v0, v73, v0
	v_exp_f32_e32 v157, v32
	v_add_f32_e32 v0, v74, v0
	v_add_f32_e32 v158, v75, v0
	v_mov_b32_e32 v159, v158
	s_nop 1
	v_permlane32_swap_b32_e32 v158, v159
	v_cmp_gt_f32_e32 vcc, 1.0, v157
	s_cbranch_vccz .LBB0_1201
; __device__ __forceinline__ int crow(int r, int hi) { return (r & 3) + 8 * (r >> 2) + 4 * hi; }
; template <int DK16, int DV32, bool MASK, int HALFWIN, bool RES, bool WT, class P>
; __device__ __forceinline__ void attn_unit(LAS unsigned char* lds, const P& c, const int ntiles, const float C, const int wv) {
;     ...
;             if (__any(alpha < 1.f)) { if (hi == 0) al_l[r32] = alpha; asm volatile("s_waitcnt lgkmcnt(0)" ::: "memory");
; #pragma unroll
;                 for (int r = 0; r < 16; ++r) { const float a = al_l[crow(r, hi)];
; #pragma unroll
;                     for (int d = 0; d < DV32; ++d) o[d][r] *= a; } }
	s_and_saveexec_b64 s[0:1], s[4:5]
	v_lshl_add_u32 v0, v156, 2, s10
	ds_write_b32 v0, v157 offset:128
	s_or_b64 exec, exec, s[0:1]
	s_waitcnt lgkmcnt(0)
	v_add_u32_e32 v8, s10, v64
	ds_read_b128 v[0:3], v8 offset:224
	ds_read_b128 v[4:7], v8 offset:192
	ds_read_b128 v[32:35], v8 offset:160
	ds_read_b128 v[36:39], v8 offset:128
	s_waitcnt lgkmcnt(3)
	v_pk_mul_f32 v[14:15], v[2:3], 0 op_sel_hi:[1,0]
	s_waitcnt lgkmcnt(2)
	v_pk_mul_f32 v[10:11], v[6:7], 0 op_sel_hi:[1,0]
	s_waitcnt lgkmcnt(1)
	v_pk_mul_f32 v[6:7], v[34:35], 0 op_sel_hi:[1,0]
	s_waitcnt lgkmcnt(0)
	v_pk_mul_f32 v[2:3], v[38:39], 0 op_sel_hi:[1,0]
	v_pk_mul_f32 v[12:13], v[0:1], 0 op_sel_hi:[1,0]
	v_pk_mul_f32 v[8:9], v[4:5], 0 op_sel_hi:[1,0]
	v_pk_mul_f32 v[4:5], v[32:33], 0 op_sel_hi:[1,0]
	v_pk_mul_f32 v[0:1], v[36:37], 0 op_sel_hi:[1,0]
	s_branch .LBB0_1202

; #define LAS __attribute__((address_space(3)))
; template <int DK16, int DV32, bool MASK, int HALFWIN, bool RES, bool WT, class P>
; __device__ __forceinline__ void attn_unit(LAS unsigned char* lds, const P& c, const int ntiles, const float C, const int wv) {
;     ...
;             const LAS unsigned char* Ks = K_lds + b * SHM_T;
;             if (do0) {
; #pragma unroll
;                 for (int d0 = 0; d0 < DK16; ++d0) { const bf16x8 b0 = *(const LAS bf16x8*)(Ks + ATT_KSWZ(r32, (d0 * 16 + hi * 8) * 2)); p0 = __builtin_amdgcn_mfma_f32_32x32x16_bf16(b0, qr[d0], p0, 0, 0, 0); } }
;     ...
;             const int vb = vb0 + b * SHM_T;
;     ...
;             if (do0) { bf16x8 pa0, pa1; ATT_PK4(p0, 0, pa0); ATT_PK4(p0, 8, pa1);
;                 pv_half2<0, 1, 0>(o[0], o[1], vb, pa0, pa1);
;                 if constexpr (DV32 == 4) { pv_half2<2, 3, 0>(o[2], o[3], vb, pa0, pa1); } }
;             if (do1) { bf16x8 pa2, pa3; ATT_PK4(p1, 0, pa2); ATT_PK4(p1, 8, pa3);
;                 pv_half2<0, 1, 1>(o[0], o[1], vb, pa2, pa3);
;                 if constexpr (DV32 == 4) { pv_half2<2, 3, 1>(o[2], o[3], vb, pa2, pa3); } }
.LBB0_1202:
	v_lshlrev_b32_e32 v33, 4, v155
	v_lshlrev_b32_e32 v32, 3, v155
	v_and_b32_e32 v33, 0xc0, v33
	v_lshlrev_b32_e32 v160, 1, v155
	v_and_or_b32 v33, v32, 24, v33
	v_and_b32_e32 v34, 32, v160
	v_and_b32_e32 v32, 0x100, v32
	v_or3_b32 v170, v33, v34, v32
	v_add_u32_e32 v96, 0x100, v170
	v_cvt_pk_bf16_f32 v76, v16, v17
	v_cvt_pk_bf16_f32 v77, v18, v19
	v_cvt_pk_bf16_f32 v78, v20, v21
	v_cvt_pk_bf16_f32 v79, v22, v23
	v_cvt_pk_bf16_f32 v80, v24, v25
	v_cvt_pk_bf16_f32 v81, v26, v27
	v_cvt_pk_bf16_f32 v82, v28, v29
	v_cvt_pk_bf16_f32 v83, v30, v31
	ds_read_b64_tr_b16 v[32:33], v96 offset:0
	ds_read_b64_tr_b16 v[34:35], v96 offset:0x800
	ds_read_b64_tr_b16 v[54:55], v96 offset:0x1000
	ds_read_b64_tr_b16 v[56:57], v96 offset:0x1800
	ds_read_b64_tr_b16 v[58:59], v96 offset:0x200
	ds_read_b64_tr_b16 v[60:61], v96 offset:0xa00
	ds_read_b64_tr_b16 v[84:85], v96 offset:0x1200
	ds_read_b64_tr_b16 v[86:87], v96 offset:0x1a00
	s_waitcnt lgkmcnt(0)
	s_nop 0
	v_permlane32_swap_b32_e32 v76, v78
	v_permlane32_swap_b32_e32 v77, v79
	v_permlane32_swap_b32_e32 v80, v82
	v_permlane32_swap_b32_e32 v81, v83
	v_mfma_f32_32x32x16_bf16 v[16:31], v[76:79], v[32:35], v[0:15]
	v_mfma_f32_32x32x16_bf16 v[32:47], v[76:79], v[58:61], v[0:15]
	v_mfma_f32_32x32x16_bf16 v[32:47], v[80:83], v[84:87], v[32:47]
	ds_read_b64_tr_b16 v[84:85], v96 offset:0x400
	ds_read_b64_tr_b16 v[86:87], v96 offset:0xc00
	ds_read_b64_tr_b16 v[88:89], v96 offset:0x1400
	ds_read_b64_tr_b16 v[90:91], v96 offset:0x1c00
	ds_read_b64_tr_b16 v[92:93], v96 offset:0x600
	ds_read_b64_tr_b16 v[94:95], v96 offset:0xe00
	ds_read_b64_tr_b16 v[138:139], v96 offset:0x1600
	v_mfma_f32_32x32x16_bf16 v[16:31], v[80:83], v[54:57], v[16:31]
	ds_read_b64_tr_b16 v[140:141], v96 offset:0x1e00
	s_waitcnt lgkmcnt(0)
	v_cvt_pk_bf16_f32 v134, v48, v49
	v_cvt_pk_bf16_f32 v135, v50, v51
	v_cvt_pk_bf16_f32 v136, v52, v53
	v_mfma_f32_32x32x16_bf16 v[48:63], v[76:79], v[84:87], v[0:15]
	v_cvt_pk_bf16_f32 v137, v66, v67
	v_cvt_pk_bf16_f32 v130, v68, v69
	v_cvt_pk_bf16_f32 v131, v70, v71
	v_cvt_pk_bf16_f32 v132, v72, v73
	v_cvt_pk_bf16_f32 v133, v74, v75
	ds_read_b64_tr_b16 v[66:67], v96 offset:0x2000
	ds_read_b64_tr_b16 v[68:69], v96 offset:0x2800
	v_mfma_f32_32x32x16_bf16 v[0:15], v[76:79], v[92:95], v[0:15]
	ds_read_b64_tr_b16 v[70:71], v96 offset:0x3000
	ds_read_b64_tr_b16 v[72:73], v96 offset:0x3800
	ds_read_b64_tr_b16 v[74:75], v96 offset:0x2200
	ds_read_b64_tr_b16 v[76:77], v96 offset:0x2a00
	ds_read_b64_tr_b16 v[84:85], v96 offset:0x3200
	ds_read_b64_tr_b16 v[86:87], v96 offset:0x3a00
	s_waitcnt lgkmcnt(0)
	v_mfma_f32_32x32x16_bf16 v[48:63], v[80:83], v[88:91], v[48:63]
	v_permlane32_swap_b32_e32 v134, v136
	v_permlane32_swap_b32_e32 v135, v137
	v_permlane32_swap_b32_e32 v130, v132
	v_permlane32_swap_b32_e32 v131, v133
	v_mfma_f32_32x32x16_bf16 v[0:15], v[80:83], v[138:141], v[0:15]
	v_mfma_f32_32x32x16_bf16 v[16:31], v[134:137], v[66:69], v[16:31]
	ds_read_b64_tr_b16 v[150:151], v96 offset:0x2400
	ds_read_b64_tr_b16 v[152:153], v96 offset:0x2c00
	ds_read_b64_tr_b16 v[142:143], v96 offset:0x3400
	ds_read_b64_tr_b16 v[144:145], v96 offset:0x3c00
	ds_read_b64_tr_b16 v[146:147], v96 offset:0x2600
	ds_read_b64_tr_b16 v[148:149], v96 offset:0x2e00
	ds_read_b64_tr_b16 v[138:139], v96 offset:0x3600
	v_mfma_f32_32x32x16_bf16 v[32:47], v[134:137], v[74:77], v[32:47]
	ds_read_b64_tr_b16 v[140:141], v96 offset:0x3e00
	s_waitcnt lgkmcnt(0)
	v_mfma_f32_32x32x16_bf16 v[16:31], v[130:133], v[70:73], v[16:31]
	v_mfma_f32_32x32x16_bf16 v[32:47], v[130:133], v[84:87], v[32:47]
	v_add_u32_e32 v176, s47, v168
	v_add_u32_e32 v86, v176, v169
	ds_read_b128 v[66:69], v86 offset:8192
	v_add_u32_e32 v172, v176, v162
	ds_read_b128 v[82:85], v172 offset:8192
	v_add_u32_e32 v177, v176, v163
	v_add_u32_e32 v178, v176, v164
	v_add_u32_e32 v179, v176, v165
	v_add_u32_e32 v180, v176, v166
	v_add_u32_e32 v181, v176, v167
	v_add_u32_e32 v176, v176, v161
	s_waitcnt lgkmcnt(1)
; template <int DK16, int DV32, bool MASK, int HALFWIN, bool RES, bool WT, class P>
; __device__ __forceinline__ void attn_unit(LAS unsigned char* lds, const P& c, const int ntiles, const float C, const int wv) {
;     ...
;             if (do0) {
; #pragma unroll
;                 for (int d0 = 0; d0 < DK16; ++d0) { const bf16x8 b0 = *(const LAS bf16x8*)(Ks + ATT_KSWZ(r32, (d0 * 16 + hi * 8) * 2)); p0 = __builtin_amdgcn_mfma_f32_32x32x16_bf16(b0, qr[d0], p0, 0, 0, 0); } }
;             if (do1) {
; #pragma unroll
;                 for (int d0 = 0; d0 < DK16; ++d0) { const bf16x8 b1 = *(const LAS bf16x8*)(Ks + ATT_KSWZ(32 + r32, (d0 * 16 + hi * 8) * 2)); p1 = __builtin_amdgcn_mfma_f32_32x32x16_bf16(b1, qr[d0], p1, 0, 0, 0); } }
;             if constexpr (MASK) {
;                 const int db = c.dbase(wid, r32, t) + 4 * hi, qi = c.qidx(wid, r32); const unsigned L = (unsigned)c.seqlen(); const bool edge = c.edge();
;                 const LAS float* tb = c.tab(wid) + (db + 2 * HALFWIN);
;     ...
;                 if (do0) ATT_XFORM(p0, 0);
;                 if (do1) ATT_XFORM(p1, 32);
;     ...
;             } else {
; #pragma unroll
;                 for (int r = 0; r < 16; ++r) { p0[r] *= C; p1[r] *= C; }
;             }
;             float pmax = -__builtin_inff();
;             if (do0) {
; #pragma unroll
;                 for (int r = 0; r < 16; ++r) pmax = fmaxf(pmax, p0[r]); }
;             if (do1) {
; #pragma unroll
;                 for (int r = 0; r < 16; ++r) pmax = fmaxf(pmax, p1[r]); }
;             { auto rr = __builtin_amdgcn_permlane32_swap(__float_as_uint(pmax), __float_as_uint(pmax), false, false);
;               pmax = fmaxf(__uint_as_float(rr[0]), __uint_as_float(rr[1])); }
;             const float mn = fmaxf(m_reg, pmax), alpha = __builtin_amdgcn_exp2f(m_reg - mn); m_reg = mn;
;             float ps = 0.f;
;             if (do0) {
; #pragma unroll
;                 for (int r = 0; r < 16; ++r) { p0[r] = __builtin_amdgcn_exp2f(p0[r] - mn); ps += p0[r]; } }
;             if (do1) {
; #pragma unroll
;                 for (int r = 0; r < 16; ++r) { p1[r] = __builtin_amdgcn_exp2f(p1[r] - mn); ps += p1[r]; } }
;             { auto rr = __builtin_amdgcn_permlane32_swap(__float_as_uint(ps), __float_as_uint(ps), false, false);
;               ps = __uint_as_float(rr[0]) + __uint_as_float(rr[1]); }
;             l_reg = l_reg * alpha + ps;
	v_mfma_f32_32x32x16_bf16 v[66:81], v[66:69], v[126:129], 0
	ds_read_b128 v[172:175], v172
	s_waitcnt lgkmcnt(1)
	v_mfma_f32_32x32x16_bf16 v[66:81], v[82:85], v[122:125], v[66:81]
	ds_read_b128 v[230:233], v177 offset:8192
	ds_read_b128 v[82:85], v178 offset:8192
	s_waitcnt lgkmcnt(1)
	v_mfma_f32_32x32x16_bf16 v[66:81], v[230:233], v[118:121], v[66:81]
	ds_read_b128 v[230:233], v179 offset:8192
	s_waitcnt lgkmcnt(1)
	v_mfma_f32_32x32x16_bf16 v[66:81], v[82:85], v[114:117], v[66:81]
	ds_read_b128 v[82:85], v180 offset:8192
	s_waitcnt lgkmcnt(1)
	v_mfma_f32_32x32x16_bf16 v[66:81], v[230:233], v[110:113], v[66:81]
	ds_read_b128 v[230:233], v181 offset:8192
	s_waitcnt lgkmcnt(1)
	v_mfma_f32_32x32x16_bf16 v[66:81], v[82:85], v[106:109], v[66:81]
	ds_read_b128 v[82:85], v86
	s_waitcnt lgkmcnt(1)
	v_mfma_f32_32x32x16_bf16 v[66:81], v[230:233], v[102:105], v[66:81]
	s_waitcnt lgkmcnt(0)
	v_mfma_f32_32x32x16_bf16 v[82:97], v[82:85], v[126:129], 0
	v_mfma_f32_32x32x16_bf16 v[82:97], v[172:175], v[122:125], v[82:97]
	ds_read_b128 v[172:175], v177
	ds_read_b128 v[230:233], v178
	s_waitcnt lgkmcnt(1)
	v_mfma_f32_32x32x16_bf16 v[82:97], v[172:175], v[118:121], v[82:97]
	ds_read_b128 v[172:175], v179
	s_waitcnt lgkmcnt(1)
	v_mfma_f32_32x32x16_bf16 v[82:97], v[230:233], v[114:117], v[82:97]
	ds_read_b128 v[230:233], v180
	s_waitcnt lgkmcnt(1)
	v_mfma_f32_32x32x16_bf16 v[82:97], v[172:175], v[110:113], v[82:97]
	ds_read_b128 v[172:175], v181
	s_waitcnt lgkmcnt(1)
	v_mfma_f32_32x32x16_bf16 v[82:97], v[230:233], v[106:109], v[82:97]
	ds_read_b128 v[230:233], v176
	s_waitcnt lgkmcnt(1)
	v_mfma_f32_32x32x16_bf16 v[82:97], v[172:175], v[102:105], v[82:97]
	ds_read_b128 v[172:175], v176 offset:8192
	s_waitcnt lgkmcnt(1)
	v_mfma_f32_32x32x16_bf16 v[82:97], v[230:233], v[98:101], v[82:97]
	s_waitcnt lgkmcnt(0)
	v_mfma_f32_32x32x16_bf16 v[66:81], v[172:175], v[98:101], v[66:81]
	s_nop 8
	v_mul_f32_e32 v176, 0x3e0293ee, v82
	v_mul_f32_e32 v173, 0x3e0293ee, v83
	v_mul_f32_e32 v175, 0x3e0293ee, v84
	v_mul_f32_e32 v178, 0x3e0293ee, v85
	v_max3_f32 v173, v176, s38, v173
	v_mul_f32_e32 v180, 0x3e0293ee, v86
	v_mul_f32_e32 v182, 0x3e0293ee, v87
	v_max3_f32 v173, v173, v175, v178
	v_mul_f32_e32 v184, 0x3e0293ee, v88
	v_mul_f32_e32 v186, 0x3e0293ee, v89
	v_max3_f32 v173, v173, v180, v182
	v_mul_f32_e32 v188, 0x3e0293ee, v90
	v_mul_f32_e32 v190, 0x3e0293ee, v91
	v_max3_f32 v173, v173, v184, v186
	v_mul_f32_e32 v192, 0x3e0293ee, v92
	v_mul_f32_e32 v194, 0x3e0293ee, v93
	v_max3_f32 v173, v173, v188, v190
	v_mul_f32_e32 v196, 0x3e0293ee, v94
	v_mul_f32_e32 v198, 0x3e0293ee, v95
	v_max3_f32 v173, v173, v192, v194
	v_mul_f32_e32 v200, 0x3e0293ee, v96
	v_mul_f32_e32 v202, 0x3e0293ee, v97
	v_max3_f32 v173, v173, v196, v198
	v_mul_f32_e32 v172, 0x3e0293ee, v66
	v_mul_f32_e32 v174, 0x3e0293ee, v67
	v_max3_f32 v173, v173, v200, v202
	v_mul_f32_e32 v177, 0x3e0293ee, v68
	v_mul_f32_e32 v179, 0x3e0293ee, v69
	v_max3_f32 v172, v173, v172, v174
	v_mul_f32_e32 v181, 0x3e0293ee, v70
	v_mul_f32_e32 v183, 0x3e0293ee, v71
	v_max3_f32 v172, v172, v177, v179
	v_mul_f32_e32 v185, 0x3e0293ee, v72
	v_mul_f32_e32 v187, 0x3e0293ee, v73
	v_max3_f32 v172, v172, v181, v183
	v_mul_f32_e32 v189, 0x3e0293ee, v74
	v_mul_f32_e32 v191, 0x3e0293ee, v75
	v_max3_f32 v172, v172, v185, v187
	v_mul_f32_e32 v193, 0x3e0293ee, v76
	v_mul_f32_e32 v195, 0x3e0293ee, v77
	v_max3_f32 v172, v172, v189, v191
	v_mul_f32_e32 v197, 0x3e0293ee, v78
	v_mul_f32_e32 v199, 0x3e0293ee, v79
	v_max3_f32 v172, v172, v193, v195
	v_mul_f32_e32 v201, 0x3e0293ee, v80
	v_mul_f32_e32 v203, 0x3e0293ee, v81
	v_max3_f32 v172, v172, v197, v199
	v_max3_f32 v172, v172, v201, v203
	v_mov_b32_e32 v173, v172
	s_nop 1
	v_permlane32_swap_b32_e32 v172, v173
	v_max3_f32 v174, v171, v172, v173
	v_sub_f32_e32 v173, v174, v171
	v_cmp_lt_f32_e32 vcc, 0x41000000, v173
	s_cbranch_vccnz .Llz_x1
	v_mov_b32_e32 v174, v171

; #define LAS __attribute__((address_space(3)))
; template <int DK16, int DV32, bool MASK, int HALFWIN, bool RES, bool WT, class P>
; __device__ __forceinline__ void attn_unit(LAS unsigned char* lds, const P& c, const int ntiles, const float C, const int wv) {
;     ...
;             const LAS unsigned char* Ks = K_lds + b * SHM_T;
;             if (do0) {
; #pragma unroll
;                 for (int d0 = 0; d0 < DK16; ++d0) { const bf16x8 b0 = *(const LAS bf16x8*)(Ks + ATT_KSWZ(r32, (d0 * 16 + hi * 8) * 2)); p0 = __builtin_amdgcn_mfma_f32_32x32x16_bf16(b0, qr[d0], p0, 0, 0, 0); } }
;     ...
;             const int vb = vb0 + b * SHM_T;
;     ...
;             if (do0) { bf16x8 pa0, pa1; ATT_PK4(p0, 0, pa0); ATT_PK4(p0, 8, pa1);
;                 pv_half2<0, 1, 0>(o[0], o[1], vb, pa0, pa1);
;                 if constexpr (DV32 == 4) { pv_half2<2, 3, 0>(o[2], o[3], vb, pa0, pa1); } }
;             if (do1) { bf16x8 pa2, pa3; ATT_PK4(p1, 0, pa2); ATT_PK4(p1, 8, pa3);
;                 pv_half2<0, 1, 1>(o[0], o[1], vb, pa2, pa3);
;                 if constexpr (DV32 == 4) { pv_half2<2, 3, 1>(o[2], o[3], vb, pa2, pa3); } }
.LBB0_1206:
	s_add_i32 s0, s59, 0x100
	v_add_u32_e32 v97, s0, v170
	v_cvt_pk_bf16_f32 v130, v175, v83
	v_cvt_pk_bf16_f32 v131, v84, v85
	v_cvt_pk_bf16_f32 v132, v86, v176
	v_cvt_pk_bf16_f32 v133, v88, v89
	v_cvt_pk_bf16_f32 v84, v87, v90
	v_cvt_pk_bf16_f32 v85, v91, v92
	v_cvt_pk_bf16_f32 v86, v93, v94
	v_cvt_pk_bf16_f32 v87, v95, v96
	ds_read_b64_tr_b16 v[88:89], v97 offset:0
	ds_read_b64_tr_b16 v[90:91], v97 offset:0x800
	ds_read_b64_tr_b16 v[92:93], v97 offset:0x1000
	ds_read_b64_tr_b16 v[94:95], v97 offset:0x1800
	ds_read_b64_tr_b16 v[134:135], v97 offset:0x200
	ds_read_b64_tr_b16 v[136:137], v97 offset:0xa00
	ds_read_b64_tr_b16 v[138:139], v97 offset:0x1200
	ds_read_b64_tr_b16 v[140:141], v97 offset:0x1a00
	s_waitcnt lgkmcnt(0)
	s_nop 0
	v_permlane32_swap_b32_e32 v84, v86
	v_permlane32_swap_b32_e32 v85, v87
	v_permlane32_swap_b32_e32 v130, v132
	v_permlane32_swap_b32_e32 v131, v133
	s_nop 1
	v_mfma_f32_32x32x16_bf16 v[16:31], v[130:133], v[88:91], v[16:31]
	ds_read_b64_tr_b16 v[88:89], v97 offset:0x400
	ds_read_b64_tr_b16 v[90:91], v97 offset:0xc00
	v_mfma_f32_32x32x16_bf16 v[32:47], v[130:133], v[134:137], v[32:47]
	v_mfma_f32_32x32x16_bf16 v[16:31], v[84:87], v[92:95], v[16:31]
	ds_read_b64_tr_b16 v[92:93], v97 offset:0x1400
	ds_read_b64_tr_b16 v[94:95], v97 offset:0x1c00
	ds_read_b64_tr_b16 v[134:135], v97 offset:0x600
	ds_read_b64_tr_b16 v[136:137], v97 offset:0xe00
	v_mfma_f32_32x32x16_bf16 v[32:47], v[84:87], v[138:141], v[32:47]
	ds_read_b64_tr_b16 v[138:139], v97 offset:0x1600
	ds_read_b64_tr_b16 v[140:141], v97 offset:0x1e00
	s_waitcnt lgkmcnt(0)
	v_mfma_f32_32x32x16_bf16 v[48:63], v[130:133], v[88:91], v[48:63]
	v_mfma_f32_32x32x16_bf16 v[0:15], v[130:133], v[134:137], v[0:15]
	v_cvt_pk_bf16_f32 v134, v66, v67
	v_cvt_pk_bf16_f32 v135, v68, v69
	v_cvt_pk_bf16_f32 v136, v70, v82
	v_cvt_pk_bf16_f32 v137, v71, v73
	v_cvt_pk_bf16_f32 v130, v72, v74
	v_cvt_pk_bf16_f32 v131, v75, v76
	v_cvt_pk_bf16_f32 v132, v77, v78
	v_cvt_pk_bf16_f32 v133, v79, v80
	ds_read_b64_tr_b16 v[66:67], v97 offset:0x2000
	ds_read_b64_tr_b16 v[68:69], v97 offset:0x2800
	ds_read_b64_tr_b16 v[70:71], v97 offset:0x3000
	v_mfma_f32_32x32x16_bf16 v[48:63], v[84:87], v[92:95], v[48:63]
	ds_read_b64_tr_b16 v[72:73], v97 offset:0x3800
	ds_read_b64_tr_b16 v[74:75], v97 offset:0x2200
	ds_read_b64_tr_b16 v[76:77], v97 offset:0x2a00
	ds_read_b64_tr_b16 v[78:79], v97 offset:0x3200
	ds_read_b64_tr_b16 v[80:81], v97 offset:0x3a00
	s_waitcnt lgkmcnt(0)
	v_permlane32_swap_b32_e32 v134, v136
	v_mfma_f32_32x32x16_bf16 v[0:15], v[84:87], v[138:141], v[0:15]
	v_permlane32_swap_b32_e32 v135, v137
	v_permlane32_swap_b32_e32 v130, v132
	v_permlane32_swap_b32_e32 v131, v133
	v_mfma_f32_32x32x16_bf16 v[16:31], v[134:137], v[66:69], v[16:31]
	ds_read_b64_tr_b16 v[150:151], v97 offset:0x2400
	ds_read_b64_tr_b16 v[152:153], v97 offset:0x2c00
	ds_read_b64_tr_b16 v[142:143], v97 offset:0x3400
	ds_read_b64_tr_b16 v[144:145], v97 offset:0x3c00
	ds_read_b64_tr_b16 v[146:147], v97 offset:0x2600
	ds_read_b64_tr_b16 v[148:149], v97 offset:0x2e00
	ds_read_b64_tr_b16 v[138:139], v97 offset:0x3600
	v_mfma_f32_32x32x16_bf16 v[32:47], v[134:137], v[74:77], v[32:47]
	ds_read_b64_tr_b16 v[140:141], v97 offset:0x3e00
	s_waitcnt lgkmcnt(0)
	v_mfma_f32_32x32x16_bf16 v[16:31], v[130:133], v[70:73], v[16:31]
	v_mfma_f32_32x32x16_bf16 v[32:47], v[130:133], v[78:81], v[32:47]
	v_add_u32_e32 v175, s52, v168
	v_add_u32_e32 v86, v175, v169
	ds_read_b128 v[66:69], v86 offset:8192
	v_add_u32_e32 v176, v175, v162
	ds_read_b128 v[82:85], v176 offset:8192
	v_add_u32_e32 v180, v175, v163
	v_add_u32_e32 v181, v175, v164
	v_add_u32_e32 v182, v175, v165
	v_add_u32_e32 v183, v175, v166
	v_add_u32_e32 v184, v175, v167
	v_add_u32_e32 v175, v175, v161
	s_waitcnt lgkmcnt(1)
; template <int DK16, int DV32, bool MASK, int HALFWIN, bool RES, bool WT, class P>
; __device__ __forceinline__ void attn_unit(LAS unsigned char* lds, const P& c, const int ntiles, const float C, const int wv) {
;     ...
;             if (do0) {
; #pragma unroll
;                 for (int d0 = 0; d0 < DK16; ++d0) { const bf16x8 b0 = *(const LAS bf16x8*)(Ks + ATT_KSWZ(r32, (d0 * 16 + hi * 8) * 2)); p0 = __builtin_amdgcn_mfma_f32_32x32x16_bf16(b0, qr[d0], p0, 0, 0, 0); } }
;             if (do1) {
; #pragma unroll
;                 for (int d0 = 0; d0 < DK16; ++d0) { const bf16x8 b1 = *(const LAS bf16x8*)(Ks + ATT_KSWZ(32 + r32, (d0 * 16 + hi * 8) * 2)); p1 = __builtin_amdgcn_mfma_f32_32x32x16_bf16(b1, qr[d0], p1, 0, 0, 0); } }
;             if constexpr (MASK) {
;                 const int db = c.dbase(wid, r32, t) + 4 * hi, qi = c.qidx(wid, r32); const unsigned L = (unsigned)c.seqlen(); const bool edge = c.edge();
;                 const LAS float* tb = c.tab(wid) + (db + 2 * HALFWIN);
;     ...
;                 if (do0) ATT_XFORM(p0, 0);
;                 if (do1) ATT_XFORM(p1, 32);
;     ...
;             } else {
; #pragma unroll
;                 for (int r = 0; r < 16; ++r) { p0[r] *= C; p1[r] *= C; }
;             }
;             float pmax = -__builtin_inff();
;             if (do0) {
; #pragma unroll
;                 for (int r = 0; r < 16; ++r) pmax = fmaxf(pmax, p0[r]); }
;             if (do1) {
; #pragma unroll
;                 for (int r = 0; r < 16; ++r) pmax = fmaxf(pmax, p1[r]); }
;             { auto rr = __builtin_amdgcn_permlane32_swap(__float_as_uint(pmax), __float_as_uint(pmax), false, false);
;               pmax = fmaxf(__uint_as_float(rr[0]), __uint_as_float(rr[1])); }
;             const float mn = fmaxf(m_reg, pmax), alpha = __builtin_amdgcn_exp2f(m_reg - mn); m_reg = mn;
;             float ps = 0.f;
;             if (do0) {
; #pragma unroll
;                 for (int r = 0; r < 16; ++r) { p0[r] = __builtin_amdgcn_exp2f(p0[r] - mn); ps += p0[r]; } }
;             if (do1) {
; #pragma unroll
;                 for (int r = 0; r < 16; ++r) { p1[r] = __builtin_amdgcn_exp2f(p1[r] - mn); ps += p1[r]; } }
;             { auto rr = __builtin_amdgcn_permlane32_swap(__float_as_uint(ps), __float_as_uint(ps), false, false);
;               ps = __uint_as_float(rr[0]) + __uint_as_float(rr[1]); }
;             l_reg = l_reg * alpha + ps;
	v_mfma_f32_32x32x16_bf16 v[66:81], v[66:69], v[126:129], 0
	ds_read_b128 v[176:179], v176
	s_waitcnt lgkmcnt(1)
	v_mfma_f32_32x32x16_bf16 v[66:81], v[82:85], v[122:125], v[66:81]
	ds_read_b128 v[230:233], v180 offset:8192
	ds_read_b128 v[82:85], v181 offset:8192
	s_waitcnt lgkmcnt(1)
	v_mfma_f32_32x32x16_bf16 v[66:81], v[230:233], v[118:121], v[66:81]
	ds_read_b128 v[230:233], v182 offset:8192
	s_waitcnt lgkmcnt(1)
	v_mfma_f32_32x32x16_bf16 v[66:81], v[82:85], v[114:117], v[66:81]
	ds_read_b128 v[82:85], v183 offset:8192
	s_waitcnt lgkmcnt(1)
	v_mfma_f32_32x32x16_bf16 v[66:81], v[230:233], v[110:113], v[66:81]
	ds_read_b128 v[230:233], v184 offset:8192
	s_waitcnt lgkmcnt(1)
	v_mfma_f32_32x32x16_bf16 v[66:81], v[82:85], v[106:109], v[66:81]
	ds_read_b128 v[82:85], v86
	s_waitcnt lgkmcnt(1)
	v_mfma_f32_32x32x16_bf16 v[66:81], v[230:233], v[102:105], v[66:81]
	s_waitcnt lgkmcnt(0)
	v_mfma_f32_32x32x16_bf16 v[82:97], v[82:85], v[126:129], 0
	v_mfma_f32_32x32x16_bf16 v[82:97], v[176:179], v[122:125], v[82:97]
	ds_read_b128 v[176:179], v180
	ds_read_b128 v[230:233], v181
	s_waitcnt lgkmcnt(1)
	v_mfma_f32_32x32x16_bf16 v[82:97], v[176:179], v[118:121], v[82:97]
	ds_read_b128 v[176:179], v182
	s_waitcnt lgkmcnt(1)
	v_mfma_f32_32x32x16_bf16 v[82:97], v[230:233], v[114:117], v[82:97]
	ds_read_b128 v[230:233], v183
	s_waitcnt lgkmcnt(1)
	v_mfma_f32_32x32x16_bf16 v[82:97], v[176:179], v[110:113], v[82:97]
	ds_read_b128 v[176:179], v184
	s_waitcnt lgkmcnt(1)
	v_mfma_f32_32x32x16_bf16 v[82:97], v[230:233], v[106:109], v[82:97]
	ds_read_b128 v[230:233], v175
	s_waitcnt lgkmcnt(1)
	v_mfma_f32_32x32x16_bf16 v[82:97], v[176:179], v[102:105], v[82:97]
	ds_read_b128 v[176:179], v175 offset:8192
	s_waitcnt lgkmcnt(1)
	v_mfma_f32_32x32x16_bf16 v[82:97], v[230:233], v[98:101], v[82:97]
	s_waitcnt lgkmcnt(0)
	v_mfma_f32_32x32x16_bf16 v[66:81], v[176:179], v[98:101], v[66:81]
	s_nop 8
	v_mul_f32_e32 v175, 0x3e0293ee, v82
	v_mul_f32_e32 v177, 0x3e0293ee, v83
	v_mul_f32_e32 v179, 0x3e0293ee, v84
	v_mul_f32_e32 v181, 0x3e0293ee, v85
	v_max3_f32 v175, v175, s38, v177
	v_mul_f32_e32 v183, 0x3e0293ee, v86
	v_mul_f32_e32 v185, 0x3e0293ee, v87
	v_max3_f32 v175, v175, v179, v181
	v_mul_f32_e32 v187, 0x3e0293ee, v88
	v_mul_f32_e32 v189, 0x3e0293ee, v89
	v_max3_f32 v175, v175, v183, v185
	v_mul_f32_e32 v191, 0x3e0293ee, v90
	v_mul_f32_e32 v193, 0x3e0293ee, v91
	v_max3_f32 v175, v175, v187, v189
	v_mul_f32_e32 v195, 0x3e0293ee, v92
	v_mul_f32_e32 v197, 0x3e0293ee, v93
	v_max3_f32 v175, v175, v191, v193
	v_mul_f32_e32 v199, 0x3e0293ee, v94
	v_mul_f32_e32 v201, 0x3e0293ee, v95
	v_max3_f32 v175, v175, v195, v197
	v_mul_f32_e32 v203, 0x3e0293ee, v96
	v_mul_f32_e32 v205, 0x3e0293ee, v97
	v_max3_f32 v175, v175, v199, v201
	v_mul_f32_e32 v176, 0x3e0293ee, v66
	v_mul_f32_e32 v178, 0x3e0293ee, v67
	v_max3_f32 v175, v175, v203, v205
	v_mul_f32_e32 v180, 0x3e0293ee, v68
	v_mul_f32_e32 v182, 0x3e0293ee, v69
	v_max3_f32 v175, v175, v176, v178
	v_mul_f32_e32 v184, 0x3e0293ee, v70
	v_mul_f32_e32 v186, 0x3e0293ee, v71
	v_max3_f32 v175, v175, v180, v182
	v_mul_f32_e32 v188, 0x3e0293ee, v72
	v_mul_f32_e32 v190, 0x3e0293ee, v73
	v_max3_f32 v175, v175, v184, v186
	v_mul_f32_e32 v192, 0x3e0293ee, v74
	v_mul_f32_e32 v194, 0x3e0293ee, v75
	v_max3_f32 v175, v175, v188, v190
	v_mul_f32_e32 v196, 0x3e0293ee, v76
	v_mul_f32_e32 v198, 0x3e0293ee, v77
	v_max3_f32 v175, v175, v192, v194
	v_mul_f32_e32 v200, 0x3e0293ee, v78
	v_mul_f32_e32 v202, 0x3e0293ee, v79
	v_max3_f32 v175, v175, v196, v198
	v_mul_f32_e32 v204, 0x3e0293ee, v80
	v_mul_f32_e32 v206, 0x3e0293ee, v81
	v_max3_f32 v175, v175, v200, v202
	v_max3_f32 v175, v175, v204, v206
	v_mov_b32_e32 v176, v175
	s_nop 1
	v_permlane32_swap_b32_e32 v175, v176
	v_max3_f32 v177, v174, v175, v176
	v_sub_f32_e32 v176, v177, v174
	v_cmp_lt_f32_e32 vcc, 0x41000000, v176
	s_cbranch_vccnz .Llz_x2
	v_mov_b32_e32 v177, v174

; #define LAS __attribute__((address_space(3)))
; template <int DK16, int DV32, bool MASK, int HALFWIN, bool RES, bool WT, class P>
; __device__ __forceinline__ void attn_unit(LAS unsigned char* lds, const P& c, const int ntiles, const float C, const int wv) {
;     ...
;             const LAS unsigned char* Ks = K_lds + b * SHM_T;
;             if (do0) {
; #pragma unroll
;                 for (int d0 = 0; d0 < DK16; ++d0) { const bf16x8 b0 = *(const LAS bf16x8*)(Ks + ATT_KSWZ(r32, (d0 * 16 + hi * 8) * 2)); p0 = __builtin_amdgcn_mfma_f32_32x32x16_bf16(b0, qr[d0], p0, 0, 0, 0); } }
;     ...
;             const int vb = vb0 + b * SHM_T;
;     ...
;             if (do0) { bf16x8 pa0, pa1; ATT_PK4(p0, 0, pa0); ATT_PK4(p0, 8, pa1);
;                 pv_half2<0, 1, 0>(o[0], o[1], vb, pa0, pa1);
;                 if constexpr (DV32 == 4) { pv_half2<2, 3, 0>(o[2], o[3], vb, pa0, pa1); } }
;             if (do1) { bf16x8 pa2, pa3; ATT_PK4(p1, 0, pa2); ATT_PK4(p1, 8, pa3);
;                 pv_half2<0, 1, 1>(o[0], o[1], vb, pa2, pa3);
;                 if constexpr (DV32 == 4) { pv_half2<2, 3, 1>(o[2], o[3], vb, pa2, pa3); } }
.LBB0_1210:
	v_readlane_b32 s0, v254, 46
	v_cvt_pk_bf16_f32 v130, v178, v83
	v_cvt_pk_bf16_f32 v131, v84, v85
	v_cvt_pk_bf16_f32 v132, v86, v179
	v_cvt_pk_bf16_f32 v133, v88, v89
	v_cvt_pk_bf16_f32 v84, v87, v90
	s_nop 1
	v_add_u32_e32 v97, s0, v170
	v_cvt_pk_bf16_f32 v85, v91, v92
	v_cvt_pk_bf16_f32 v86, v93, v94
	v_cvt_pk_bf16_f32 v87, v95, v96
	ds_read_b64_tr_b16 v[88:89], v97 offset:0
	ds_read_b64_tr_b16 v[90:91], v97 offset:0x800
	ds_read_b64_tr_b16 v[92:93], v97 offset:0x1000
	ds_read_b64_tr_b16 v[94:95], v97 offset:0x1800
	ds_read_b64_tr_b16 v[134:135], v97 offset:0x200
	ds_read_b64_tr_b16 v[136:137], v97 offset:0xa00
	ds_read_b64_tr_b16 v[138:139], v97 offset:0x1200
	ds_read_b64_tr_b16 v[140:141], v97 offset:0x1a00
	s_waitcnt lgkmcnt(0)
	s_nop 0
	v_permlane32_swap_b32_e32 v84, v86
	v_permlane32_swap_b32_e32 v85, v87
	v_permlane32_swap_b32_e32 v130, v132
	v_permlane32_swap_b32_e32 v131, v133
	s_nop 1
	v_mfma_f32_32x32x16_bf16 v[16:31], v[130:133], v[88:91], v[16:31]
	ds_read_b64_tr_b16 v[88:89], v97 offset:0x400
	ds_read_b64_tr_b16 v[90:91], v97 offset:0xc00
	v_mfma_f32_32x32x16_bf16 v[32:47], v[130:133], v[134:137], v[32:47]
	v_mfma_f32_32x32x16_bf16 v[16:31], v[84:87], v[92:95], v[16:31]
	ds_read_b64_tr_b16 v[92:93], v97 offset:0x1400
	ds_read_b64_tr_b16 v[94:95], v97 offset:0x1c00
	ds_read_b64_tr_b16 v[134:135], v97 offset:0x600
	ds_read_b64_tr_b16 v[136:137], v97 offset:0xe00
	v_mfma_f32_32x32x16_bf16 v[32:47], v[84:87], v[138:141], v[32:47]
	ds_read_b64_tr_b16 v[138:139], v97 offset:0x1600
	ds_read_b64_tr_b16 v[140:141], v97 offset:0x1e00
	s_waitcnt lgkmcnt(0)
	v_mfma_f32_32x32x16_bf16 v[48:63], v[130:133], v[88:91], v[48:63]
	v_mfma_f32_32x32x16_bf16 v[0:15], v[130:133], v[134:137], v[0:15]
	v_cvt_pk_bf16_f32 v130, v66, v67
	v_cvt_pk_bf16_f32 v131, v68, v69
	v_cvt_pk_bf16_f32 v132, v70, v82
	v_cvt_pk_bf16_f32 v133, v71, v73
	v_cvt_pk_bf16_f32 v134, v72, v74
	v_cvt_pk_bf16_f32 v135, v75, v76
	v_cvt_pk_bf16_f32 v136, v77, v78
	v_cvt_pk_bf16_f32 v137, v79, v80
	ds_read_b64_tr_b16 v[66:67], v97 offset:0x2000
	ds_read_b64_tr_b16 v[68:69], v97 offset:0x2800
	ds_read_b64_tr_b16 v[70:71], v97 offset:0x3000
	v_mfma_f32_32x32x16_bf16 v[48:63], v[84:87], v[92:95], v[48:63]
	ds_read_b64_tr_b16 v[72:73], v97 offset:0x3800
	ds_read_b64_tr_b16 v[74:75], v97 offset:0x2200
	ds_read_b64_tr_b16 v[76:77], v97 offset:0x2a00
	ds_read_b64_tr_b16 v[78:79], v97 offset:0x3200
	ds_read_b64_tr_b16 v[80:81], v97 offset:0x3a00
	s_waitcnt lgkmcnt(0)
	v_permlane32_swap_b32_e32 v130, v132
	v_mfma_f32_32x32x16_bf16 v[0:15], v[84:87], v[138:141], v[0:15]
	v_permlane32_swap_b32_e32 v131, v133
	v_permlane32_swap_b32_e32 v134, v136
	v_permlane32_swap_b32_e32 v135, v137
	v_mfma_f32_32x32x16_bf16 v[16:31], v[130:133], v[66:69], v[16:31]
	ds_read_b64_tr_b16 v[150:151], v97 offset:0x2400
	ds_read_b64_tr_b16 v[152:153], v97 offset:0x2c00
	ds_read_b64_tr_b16 v[142:143], v97 offset:0x3400
	ds_read_b64_tr_b16 v[144:145], v97 offset:0x3c00
	ds_read_b64_tr_b16 v[146:147], v97 offset:0x2600
	ds_read_b64_tr_b16 v[148:149], v97 offset:0x2e00
	ds_read_b64_tr_b16 v[138:139], v97 offset:0x3600
	v_mfma_f32_32x32x16_bf16 v[32:47], v[130:133], v[74:77], v[32:47]
	ds_read_b64_tr_b16 v[140:141], v97 offset:0x3e00
	s_waitcnt lgkmcnt(0)
	v_mfma_f32_32x32x16_bf16 v[16:31], v[134:137], v[70:73], v[16:31]
	v_mfma_f32_32x32x16_bf16 v[32:47], v[134:137], v[78:81], v[32:47]
	v_add_u32_e32 v168, s53, v168
	v_add_u32_e32 v86, v168, v169
	ds_read_b128 v[66:69], v86 offset:8192
	v_add_u32_e32 v162, v168, v162
	ds_read_b128 v[82:85], v162 offset:8192
	v_add_u32_e32 v163, v168, v163
	v_add_u32_e32 v164, v168, v164
	v_add_u32_e32 v165, v168, v165
	v_add_u32_e32 v166, v168, v166
	v_add_u32_e32 v167, v168, v167
	v_mfma_f32_32x32x16_bf16 v[48:63], v[130:133], v[150:153], v[48:63]
	s_waitcnt lgkmcnt(1)
; template <int DK16, int DV32, bool MASK, int HALFWIN, bool RES, bool WT, class P>
; __device__ __forceinline__ void attn_unit(LAS unsigned char* lds, const P& c, const int ntiles, const float C, const int wv) {
;     ...
;             if (do0) {
; #pragma unroll
;                 for (int d0 = 0; d0 < DK16; ++d0) { const bf16x8 b0 = *(const LAS bf16x8*)(Ks + ATT_KSWZ(r32, (d0 * 16 + hi * 8) * 2)); p0 = __builtin_amdgcn_mfma_f32_32x32x16_bf16(b0, qr[d0], p0, 0, 0, 0); } }
;             if (do1) {
; #pragma unroll
;                 for (int d0 = 0; d0 < DK16; ++d0) { const bf16x8 b1 = *(const LAS bf16x8*)(Ks + ATT_KSWZ(32 + r32, (d0 * 16 + hi * 8) * 2)); p1 = __builtin_amdgcn_mfma_f32_32x32x16_bf16(b1, qr[d0], p1, 0, 0, 0); } }
;             if constexpr (MASK) {
;                 const int db = c.dbase(wid, r32, t) + 4 * hi, qi = c.qidx(wid, r32); const unsigned L = (unsigned)c.seqlen(); const bool edge = c.edge();
;                 const LAS float* tb = c.tab(wid) + (db + 2 * HALFWIN);
;     ...
;                 if (do0) ATT_XFORM(p0, 0);
;                 if (do1) ATT_XFORM(p1, 32);
;     ...
;             } else {
; #pragma unroll
;                 for (int r = 0; r < 16; ++r) { p0[r] *= C; p1[r] *= C; }
;             }
;             float pmax = -__builtin_inff();
;             if (do0) {
; #pragma unroll
;                 for (int r = 0; r < 16; ++r) pmax = fmaxf(pmax, p0[r]); }
;             if (do1) {
; #pragma unroll
;                 for (int r = 0; r < 16; ++r) pmax = fmaxf(pmax, p1[r]); }
;             { auto rr = __builtin_amdgcn_permlane32_swap(__float_as_uint(pmax), __float_as_uint(pmax), false, false);
;               pmax = fmaxf(__uint_as_float(rr[0]), __uint_as_float(rr[1])); }
;             const float mn = fmaxf(m_reg, pmax), alpha = __builtin_amdgcn_exp2f(m_reg - mn); m_reg = mn;
;             float ps = 0.f;
;             if (do0) {
; #pragma unroll
;                 for (int r = 0; r < 16; ++r) { p0[r] = __builtin_amdgcn_exp2f(p0[r] - mn); ps += p0[r]; } }
;             if (do1) {
; #pragma unroll
;                 for (int r = 0; r < 16; ++r) { p1[r] = __builtin_amdgcn_exp2f(p1[r] - mn); ps += p1[r]; } }
;             { auto rr = __builtin_amdgcn_permlane32_swap(__float_as_uint(ps), __float_as_uint(ps), false, false);
;               ps = __uint_as_float(rr[0]) + __uint_as_float(rr[1]); }
;             l_reg = l_reg * alpha + ps;
	v_mfma_f32_32x32x16_bf16 v[66:81], v[66:69], v[126:129], 0
	s_waitcnt lgkmcnt(0)
	v_mfma_f32_32x32x16_bf16 v[66:81], v[82:85], v[122:125], v[66:81]
	ds_read_b128 v[230:233], v163 offset:8192
	ds_read_b128 v[82:85], v164 offset:8192
	s_waitcnt lgkmcnt(1)
	v_mfma_f32_32x32x16_bf16 v[66:81], v[230:233], v[118:121], v[66:81]
	ds_read_b128 v[230:233], v165 offset:8192
	s_waitcnt lgkmcnt(1)
	v_mfma_f32_32x32x16_bf16 v[66:81], v[82:85], v[114:117], v[66:81]
	ds_read_b128 v[82:85], v166 offset:8192
	s_waitcnt lgkmcnt(1)
	v_mfma_f32_32x32x16_bf16 v[66:81], v[230:233], v[110:113], v[66:81]
	ds_read_b128 v[230:233], v167 offset:8192
	s_waitcnt lgkmcnt(1)
	v_mfma_f32_32x32x16_bf16 v[66:81], v[82:85], v[106:109], v[66:81]
	ds_read_b128 v[82:85], v86
	s_waitcnt lgkmcnt(1)
	v_mfma_f32_32x32x16_bf16 v[66:81], v[230:233], v[102:105], v[66:81]
	s_waitcnt lgkmcnt(0)
	v_mfma_f32_32x32x16_bf16 v[82:97], v[82:85], v[126:129], 0
	ds_read_b128 v[126:129], v162
	s_waitcnt lgkmcnt(0)
	v_mfma_f32_32x32x16_bf16 v[82:97], v[126:129], v[122:125], v[82:97]
	ds_read_b128 v[122:125], v163
	s_waitcnt lgkmcnt(0)
	v_mfma_f32_32x32x16_bf16 v[82:97], v[122:125], v[118:121], v[82:97]
	ds_read_b128 v[118:121], v164
	s_waitcnt lgkmcnt(0)
	v_mfma_f32_32x32x16_bf16 v[82:97], v[118:121], v[114:117], v[82:97]
	ds_read_b128 v[114:117], v165
	s_waitcnt lgkmcnt(0)
	v_mfma_f32_32x32x16_bf16 v[82:97], v[114:117], v[110:113], v[82:97]
	ds_read_b128 v[110:113], v166
	s_waitcnt lgkmcnt(0)
	v_mfma_f32_32x32x16_bf16 v[82:97], v[110:113], v[106:109], v[82:97]
	ds_read_b128 v[106:109], v167
	v_add_u32_e32 v110, v168, v161
	s_waitcnt lgkmcnt(0)
	v_mfma_f32_32x32x16_bf16 v[82:97], v[106:109], v[102:105], v[82:97]
	ds_read_b128 v[102:105], v110
	ds_read_b128 v[106:109], v110 offset:8192
	s_waitcnt lgkmcnt(1)
	v_mfma_f32_32x32x16_bf16 v[82:97], v[102:105], v[98:101], v[82:97]
	s_waitcnt lgkmcnt(0)
	v_mfma_f32_32x32x16_bf16 v[66:81], v[106:109], v[98:101], v[66:81]
	s_nop 9
	v_mul_f32_e32 v102, 0x3e0293ee, v82
	v_mul_f32_e32 v99, 0x3e0293ee, v83
	v_mul_f32_e32 v101, 0x3e0293ee, v84
	v_mul_f32_e32 v104, 0x3e0293ee, v85
	v_max3_f32 v99, v102, s38, v99
	v_mul_f32_e32 v106, 0x3e0293ee, v86
	v_mul_f32_e32 v108, 0x3e0293ee, v87
	v_max3_f32 v99, v99, v101, v104
	v_mul_f32_e32 v110, 0x3e0293ee, v88
	v_mul_f32_e32 v112, 0x3e0293ee, v89
	v_max3_f32 v99, v99, v106, v108
	v_mul_f32_e32 v114, 0x3e0293ee, v90
	v_mul_f32_e32 v116, 0x3e0293ee, v91
	v_max3_f32 v99, v99, v110, v112
	v_mul_f32_e32 v118, 0x3e0293ee, v92
	v_mul_f32_e32 v120, 0x3e0293ee, v93
	v_max3_f32 v99, v99, v114, v116
	v_mul_f32_e32 v122, 0x3e0293ee, v94
	v_mul_f32_e32 v124, 0x3e0293ee, v95
	v_max3_f32 v99, v99, v118, v120
	v_mul_f32_e32 v126, 0x3e0293ee, v96
	v_mul_f32_e32 v128, 0x3e0293ee, v97
	v_max3_f32 v99, v99, v122, v124
	v_mul_f32_e32 v98, 0x3e0293ee, v66
	v_mul_f32_e32 v100, 0x3e0293ee, v67
	v_max3_f32 v99, v99, v126, v128
	v_mul_f32_e32 v103, 0x3e0293ee, v68
	v_mul_f32_e32 v105, 0x3e0293ee, v69
	v_max3_f32 v98, v99, v98, v100
	v_mul_f32_e32 v107, 0x3e0293ee, v70
	v_mul_f32_e32 v109, 0x3e0293ee, v71
	v_max3_f32 v98, v98, v103, v105
	v_mul_f32_e32 v111, 0x3e0293ee, v72
	v_mul_f32_e32 v113, 0x3e0293ee, v73
	v_max3_f32 v98, v98, v107, v109
	v_mul_f32_e32 v115, 0x3e0293ee, v74
	v_mul_f32_e32 v117, 0x3e0293ee, v75
	v_max3_f32 v98, v98, v111, v113
	v_mul_f32_e32 v119, 0x3e0293ee, v76
	v_mul_f32_e32 v121, 0x3e0293ee, v77
	v_max3_f32 v98, v98, v115, v117
	v_mul_f32_e32 v123, 0x3e0293ee, v78
	v_mul_f32_e32 v125, 0x3e0293ee, v79
	v_max3_f32 v98, v98, v119, v121
	v_mul_f32_e32 v127, 0x3e0293ee, v80
	v_mul_f32_e32 v129, 0x3e0293ee, v81
	v_max3_f32 v98, v98, v123, v125
	v_max3_f32 v98, v98, v127, v129
	v_mov_b32_e32 v99, v98
	s_nop 1
	v_permlane32_swap_b32_e32 v98, v99
	v_max3_f32 v106, v177, v98, v99
	v_sub_f32_e32 v99, v106, v177
	v_cmp_lt_f32_e32 vcc, 0x41000000, v99
	s_cbranch_vccnz .Llz_x3
	v_mov_b32_e32 v106, v177
